# merge link epilogue: the 1/255 gate scale applied once per output tile instead of per link (drops 32 v_pk_mul + 32 s_nop per link; same f32 math, reassociated)
# speedup vs baseline: 1.0027x; 1.0027x over previous
.LBB0_2046:
	v_pk_mul_f32 v[130:131], v[130:131], s[84:85] op_sel_hi:[1,0]
	v_pk_mul_f32 v[128:129], v[128:129], s[84:85] op_sel_hi:[1,0]
	v_pk_mul_f32 v[126:127], v[126:127], s[84:85] op_sel_hi:[1,0]
	v_pk_mul_f32 v[124:125], v[124:125], s[84:85] op_sel_hi:[1,0]
	v_pk_mul_f32 v[122:123], v[122:123], s[84:85] op_sel_hi:[1,0]
	v_pk_mul_f32 v[120:121], v[120:121], s[84:85] op_sel_hi:[1,0]
	v_pk_mul_f32 v[118:119], v[118:119], s[84:85] op_sel_hi:[1,0]
	v_pk_mul_f32 v[116:117], v[116:117], s[84:85] op_sel_hi:[1,0]
	v_pk_mul_f32 v[114:115], v[114:115], s[84:85] op_sel_hi:[1,0]
	v_pk_mul_f32 v[112:113], v[112:113], s[84:85] op_sel_hi:[1,0]
	v_pk_mul_f32 v[110:111], v[110:111], s[84:85] op_sel_hi:[1,0]
	v_pk_mul_f32 v[108:109], v[108:109], s[84:85] op_sel_hi:[1,0]
	v_pk_mul_f32 v[106:107], v[106:107], s[84:85] op_sel_hi:[1,0]
	v_pk_mul_f32 v[104:105], v[104:105], s[84:85] op_sel_hi:[1,0]
	v_pk_mul_f32 v[102:103], v[102:103], s[84:85] op_sel_hi:[1,0]
	v_pk_mul_f32 v[100:101], v[100:101], s[84:85] op_sel_hi:[1,0]
	v_pk_mul_f32 v[98:99], v[98:99], s[84:85] op_sel_hi:[1,0]
	v_pk_mul_f32 v[96:97], v[96:97], s[84:85] op_sel_hi:[1,0]
	v_pk_mul_f32 v[94:95], v[94:95], s[84:85] op_sel_hi:[1,0]
	v_pk_mul_f32 v[92:93], v[92:93], s[84:85] op_sel_hi:[1,0]
	v_pk_mul_f32 v[90:91], v[90:91], s[84:85] op_sel_hi:[1,0]
	v_pk_mul_f32 v[88:89], v[88:89], s[84:85] op_sel_hi:[1,0]
	v_pk_mul_f32 v[86:87], v[86:87], s[84:85] op_sel_hi:[1,0]
	v_pk_mul_f32 v[84:85], v[84:85], s[84:85] op_sel_hi:[1,0]
	v_pk_mul_f32 v[82:83], v[82:83], s[84:85] op_sel_hi:[1,0]
	v_pk_mul_f32 v[80:81], v[80:81], s[84:85] op_sel_hi:[1,0]
	v_pk_mul_f32 v[78:79], v[78:79], s[84:85] op_sel_hi:[1,0]
	v_pk_mul_f32 v[76:77], v[76:77], s[84:85] op_sel_hi:[1,0]
	v_pk_mul_f32 v[74:75], v[74:75], s[84:85] op_sel_hi:[1,0]
	v_pk_mul_f32 v[72:73], v[72:73], s[84:85] op_sel_hi:[1,0]
	v_pk_mul_f32 v[70:71], v[70:71], s[84:85] op_sel_hi:[1,0]
	v_pk_mul_f32 v[68:69], v[68:69], s[84:85] op_sel_hi:[1,0]
	s_lshl_b64 s[10:11], s[10:11], 1
	s_add_u32 s10, s56, s10
	v_bfe_u32 v2, v2, 4, 2
	s_addc_u32 s11, s57, s11
	v_or_b32_e32 v4, s42, v141
	v_lshl_or_b32 v2, v2, 3, s44
	s_add_u32 s10, s10, 0x1200
	s_movk_i32 s14, 0x1200
	s_addc_u32 s11, s11, 0
	v_mul_lo_u32 v8, v4, s14
	v_mov_b32_e32 v9, v3
	v_lshl_add_u64 v[4:5], v[8:9], 1, s[10:11]
	v_lshlrev_b64 v[10:11], 1, v[2:3]
	v_lshl_add_u64 v[12:13], v[4:5], 0, v[10:11]
	v_cvt_pk_bf16_f32 v4, v128, v129
	v_cvt_pk_bf16_f32 v5, v130, v131
	v_cvt_pk_bf16_f32 v6, v124, v125
	v_cvt_pk_bf16_f32 v7, v126, v127
	global_store_dwordx4 v[12:13], v[4:7], off
	v_add_u32_e32 v2, 0x12000, v8
	s_and_b64 vcc, exec, s[8:9]
	v_cvt_pk_bf16_f32 v4, v120, v121
	v_cvt_pk_bf16_f32 v5, v122, v123
	v_cvt_pk_bf16_f32 v6, v116, v117
	v_cvt_pk_bf16_f32 v7, v118, v119
	global_store_dwordx4 v[12:13], v[4:7], off offset:64
	s_nop 1
	v_lshl_add_u64 v[4:5], v[2:3], 1, s[10:11]
	v_lshl_add_u64 v[12:13], v[4:5], 0, v[10:11]
	v_cvt_pk_bf16_f32 v4, v112, v113
	v_cvt_pk_bf16_f32 v5, v114, v115
	v_cvt_pk_bf16_f32 v6, v108, v109
	v_cvt_pk_bf16_f32 v7, v110, v111
	global_store_dwordx4 v[12:13], v[4:7], off
	v_add_u32_e32 v2, 0x24000, v8
	s_nop 0
	v_cvt_pk_bf16_f32 v4, v104, v105
	v_cvt_pk_bf16_f32 v5, v106, v107
	v_cvt_pk_bf16_f32 v6, v100, v101
	v_cvt_pk_bf16_f32 v7, v102, v103
	global_store_dwordx4 v[12:13], v[4:7], off offset:64
	s_nop 1
	v_lshl_add_u64 v[4:5], v[2:3], 1, s[10:11]
	v_lshl_add_u64 v[12:13], v[4:5], 0, v[10:11]
	v_cvt_pk_bf16_f32 v4, v96, v97
	v_cvt_pk_bf16_f32 v5, v98, v99
	v_cvt_pk_bf16_f32 v6, v92, v93
	v_cvt_pk_bf16_f32 v7, v94, v95
	global_store_dwordx4 v[12:13], v[4:7], off
	v_add_u32_e32 v2, 0x36000, v8
	s_nop 0
	v_cvt_pk_bf16_f32 v4, v88, v89
	v_cvt_pk_bf16_f32 v5, v90, v91
	v_cvt_pk_bf16_f32 v6, v84, v85
	v_cvt_pk_bf16_f32 v7, v86, v87
	global_store_dwordx4 v[12:13], v[4:7], off offset:64
	s_nop 1
	v_lshl_add_u64 v[4:5], v[2:3], 1, s[10:11]
	v_lshl_add_u64 v[8:9], v[4:5], 0, v[10:11]
	v_cvt_pk_bf16_f32 v4, v80, v81
	v_cvt_pk_bf16_f32 v5, v82, v83
	v_cvt_pk_bf16_f32 v6, v76, v77
	v_cvt_pk_bf16_f32 v7, v78, v79
	global_store_dwordx4 v[8:9], v[4:7], off
	s_nop 1
	v_cvt_pk_bf16_f32 v4, v72, v73
	v_cvt_pk_bf16_f32 v5, v74, v75
	v_cvt_pk_bf16_f32 v6, v68, v69
	v_cvt_pk_bf16_f32 v7, v70, v71
	global_store_dwordx4 v[8:9], v[4:7], off offset:64
	s_barrier
	s_cbranch_vccnz .LBB0_2074

.LBB0_2048:
	v_mov_b32_e32 v2, v132
	s_add_i32 s16, 0, 0x1e000
	v_and_b32_e32 v141, 15, v2
	v_lshlrev_b32_e32 v142, 3, v2
	v_and_b32_e32 v142, 0x100, v142
	v_or_b32_e32 v143, s43, v141
	v_add_lshl_u32 v142, v143, v142, 4
	v_lshrrev_b32_e32 v143, 1, v2
	v_and_b32_e32 v143, 8, v143
	v_add3_u32 v148, s16, v142, v143
	ds_read2_b64 v[142:145], v148 offset1:32
	s_add_i32 s55, s55, 1
	s_cmp_eq_u32 s55, 4
	s_mov_b64 s[16:17], -1
	s_waitcnt lgkmcnt(0)
	v_cvt_f32_ubyte1_e32 v147, v142
	v_cvt_f32_ubyte0_e32 v146, v142
	v_pk_fma_f32 v[128:129], v[64:65], v[146:147], v[128:129]
	v_cvt_f32_ubyte3_e32 v65, v142
	v_cvt_f32_ubyte2_e32 v64, v142
	v_add_u32_e32 v142, 0x2000, v148
	v_pk_fma_f32 v[130:131], v[66:67], v[64:65], v[130:131]
	v_cvt_f32_ubyte1_e32 v65, v143
	v_cvt_f32_ubyte0_e32 v64, v143
	v_pk_fma_f32 v[124:125], v[60:61], v[64:65], v[124:125]
	ds_read2_b64 v[64:67], v142 offset1:32
	v_cvt_f32_ubyte3_e32 v61, v143
	v_cvt_f32_ubyte2_e32 v60, v143
	v_pk_fma_f32 v[126:127], v[62:63], v[60:61], v[126:127]
	s_waitcnt lgkmcnt(0)
	v_cvt_f32_ubyte1_e32 v61, v64
	v_cvt_f32_ubyte0_e32 v60, v64
	v_pk_fma_f32 v[120:121], v[56:57], v[60:61], v[120:121]
	v_cvt_f32_ubyte3_e32 v57, v64
	v_cvt_f32_ubyte2_e32 v56, v64
	v_pk_fma_f32 v[122:123], v[58:59], v[56:57], v[122:123]
	v_cvt_f32_ubyte1_e32 v57, v65
	v_cvt_f32_ubyte0_e32 v56, v65
	v_pk_fma_f32 v[116:117], v[52:53], v[56:57], v[116:117]
	v_cvt_f32_ubyte3_e32 v53, v65
	v_cvt_f32_ubyte2_e32 v52, v65
	v_pk_fma_f32 v[118:119], v[54:55], v[52:53], v[118:119]
	v_cvt_f32_ubyte1_e32 v53, v144
	v_cvt_f32_ubyte0_e32 v52, v144
	v_pk_fma_f32 v[112:113], v[48:49], v[52:53], v[112:113]
	v_cvt_f32_ubyte3_e32 v49, v144
	v_cvt_f32_ubyte2_e32 v48, v144
	v_pk_fma_f32 v[114:115], v[50:51], v[48:49], v[114:115]
	v_cvt_f32_ubyte1_e32 v49, v145
	v_cvt_f32_ubyte0_e32 v48, v145
	v_pk_fma_f32 v[108:109], v[44:45], v[48:49], v[108:109]
	v_cvt_f32_ubyte3_e32 v45, v145
	v_cvt_f32_ubyte2_e32 v44, v145
	v_pk_fma_f32 v[110:111], v[46:47], v[44:45], v[110:111]
	v_cvt_f32_ubyte1_e32 v45, v66
	v_cvt_f32_ubyte0_e32 v44, v66
	v_pk_fma_f32 v[104:105], v[40:41], v[44:45], v[104:105]
	v_cvt_f32_ubyte3_e32 v41, v66
	v_cvt_f32_ubyte2_e32 v40, v66
	v_pk_fma_f32 v[106:107], v[42:43], v[40:41], v[106:107]
	v_cvt_f32_ubyte1_e32 v41, v67
	v_cvt_f32_ubyte0_e32 v40, v67
	v_pk_fma_f32 v[100:101], v[36:37], v[40:41], v[100:101]
	ds_read2_b64 v[40:43], v148 offset0:64 offset1:96
	v_cvt_f32_ubyte3_e32 v37, v67
	v_cvt_f32_ubyte2_e32 v36, v67
	v_pk_fma_f32 v[102:103], v[38:39], v[36:37], v[102:103]
	s_waitcnt lgkmcnt(0)
	v_cvt_f32_ubyte1_e32 v37, v40
	v_cvt_f32_ubyte0_e32 v36, v40
	v_pk_fma_f32 v[96:97], v[32:33], v[36:37], v[96:97]
	v_cvt_f32_ubyte3_e32 v33, v40
	v_cvt_f32_ubyte2_e32 v32, v40
	v_pk_fma_f32 v[98:99], v[34:35], v[32:33], v[98:99]
	v_cvt_f32_ubyte1_e32 v33, v41
	v_cvt_f32_ubyte0_e32 v32, v41
	v_pk_fma_f32 v[92:93], v[28:29], v[32:33], v[92:93]
	ds_read2_b64 v[32:35], v142 offset0:64 offset1:96
	v_cvt_f32_ubyte3_e32 v29, v41
	v_cvt_f32_ubyte2_e32 v28, v41
	v_pk_fma_f32 v[94:95], v[30:31], v[28:29], v[94:95]
	s_waitcnt lgkmcnt(0)
	v_cvt_f32_ubyte1_e32 v29, v32
	v_cvt_f32_ubyte0_e32 v28, v32
	v_pk_fma_f32 v[88:89], v[24:25], v[28:29], v[88:89]
	v_cvt_f32_ubyte3_e32 v25, v32
	v_cvt_f32_ubyte2_e32 v24, v32
	v_pk_fma_f32 v[90:91], v[26:27], v[24:25], v[90:91]
	v_cvt_f32_ubyte1_e32 v25, v33
	v_cvt_f32_ubyte0_e32 v24, v33
	v_pk_fma_f32 v[84:85], v[20:21], v[24:25], v[84:85]
	v_cvt_f32_ubyte3_e32 v21, v33
	v_cvt_f32_ubyte2_e32 v20, v33
	v_pk_fma_f32 v[86:87], v[22:23], v[20:21], v[86:87]
	v_cvt_f32_ubyte1_e32 v21, v42
	v_cvt_f32_ubyte0_e32 v20, v42
	v_pk_fma_f32 v[80:81], v[16:17], v[20:21], v[80:81]
	v_cvt_f32_ubyte3_e32 v17, v42
	v_cvt_f32_ubyte2_e32 v16, v42
	v_pk_fma_f32 v[82:83], v[18:19], v[16:17], v[82:83]
	v_cvt_f32_ubyte1_e32 v17, v43
	v_cvt_f32_ubyte0_e32 v16, v43
	v_pk_fma_f32 v[76:77], v[12:13], v[16:17], v[76:77]
	v_cvt_f32_ubyte3_e32 v13, v43
	v_cvt_f32_ubyte2_e32 v12, v43
	v_pk_fma_f32 v[78:79], v[14:15], v[12:13], v[78:79]
	v_cvt_f32_ubyte1_e32 v13, v34
	v_cvt_f32_ubyte0_e32 v12, v34
	v_pk_fma_f32 v[72:73], v[8:9], v[12:13], v[72:73]
	v_cvt_f32_ubyte3_e32 v9, v34
	v_cvt_f32_ubyte2_e32 v8, v34
	v_pk_fma_f32 v[74:75], v[10:11], v[8:9], v[74:75]
	v_cvt_f32_ubyte1_e32 v9, v35
	v_cvt_f32_ubyte0_e32 v8, v35
	v_pk_fma_f32 v[68:69], v[4:5], v[8:9], v[68:69]
	v_cvt_f32_ubyte3_e32 v5, v35
	v_cvt_f32_ubyte2_e32 v4, v35
	v_pk_fma_f32 v[70:71], v[6:7], v[4:5], v[70:71]
	s_cbranch_scc1 .LBB0_2046
